# sliding-window pooling loops (both layers): the 12 independent row loads of an iteration issued together up front with counted waits instead of 12 serial load+vmcnt(0) round trips
# speedup vs baseline: 1.0057x; 1.0057x over previous
.LBB0_640:
	v_lshl_add_u64 v[20:21], v[68:69], 0, v[122:123]
	v_add_co_u32_e32 v18, vcc, 0x34401000, v20
	v_add_u32_e32 v25, s52, v23
	s_nop 0
	v_addc_co_u32_e32 v19, vcc, 0, v21, vcc
	global_load_dwordx4 v[28:31], v[18:19], off
	v_add_co_u32_e32 v184, vcc, 0x34402000, v20
	s_nop 1
	v_addc_co_u32_e32 v185, vcc, 0, v21, vcc
	global_load_dwordx4 v[188:191], v[184:185], off offset:3584
	v_add_co_u32_e32 v184, vcc, 0x34404000, v20
	s_nop 1
	v_addc_co_u32_e32 v185, vcc, 0, v21, vcc
	global_load_dwordx4 v[192:195], v[184:185], off offset:3072
	v_add_co_u32_e32 v184, vcc, 0x34406000, v20
	s_nop 1
	v_addc_co_u32_e32 v185, vcc, 0, v21, vcc
	global_load_dwordx4 v[196:199], v[184:185], off offset:2560
	v_lshl_add_u64 v[184:185], v[16:17], 0, v[122:123]
	global_load_dwordx4 v[200:203], v[184:185], off
	v_lshl_add_u64 v[184:185], v[14:15], 0, v[122:123]
	global_load_dwordx4 v[204:207], v[184:185], off
	v_lshl_add_u64 v[184:185], v[12:13], 0, v[122:123]
	global_load_dwordx4 v[208:211], v[184:185], off
	v_lshl_add_u64 v[184:185], v[10:11], 0, v[122:123]
	global_load_dwordx4 v[212:215], v[184:185], off
	v_max_i32_e32 v186, 0, v25
	v_mad_u64_u32 v[184:185], s[54:55], v186, s42, v[66:67]
	global_load_dwordx4 v[216:219], v[184:185], off
	v_add_u32_e32 v186, 1, v25
	v_max_i32_e32 v186, 0, v186
	v_mad_u64_u32 v[184:185], s[54:55], v186, s42, v[66:67]
	global_load_dwordx4 v[220:223], v[184:185], off
	v_add_u32_e32 v186, 2, v25
	v_max_i32_e32 v186, 0, v186
	v_mad_u64_u32 v[184:185], s[54:55], v186, s42, v[66:67]
	global_load_dwordx4 v[224:227], v[184:185], off
	v_add_u32_e32 v186, 3, v25
	v_max_i32_e32 v186, 0, v186
	v_mad_u64_u32 v[184:185], s[54:55], v186, s42, v[66:67]
	global_load_dwordx4 v[228:231], v[184:185], off
	v_add_u32_e32 v24, s52, v22
	v_max_i32_e32 v27, 0, v25
	v_min_i32_e32 v32, v24, v74
	v_sub_u32_e32 v27, v32, v27
	v_cvt_f32_i32_e32 v27, v27
	v_lshl_add_u64 v[18:19], v[70:71], 0, v[122:123]
	v_add_co_u32_e32 v32, vcc, 0xfd00000, v18
	v_rcp_iflag_f32_e32 v27, v27
	v_add_u32_e32 v26, 1, v24
	v_addc_co_u32_e32 v33, vcc, 0, v19, vcc
	v_cmp_le_i32_e32 vcc, v26, v74
	s_waitcnt vmcnt(11)
	v_lshlrev_b32_e32 v34, 16, v28
	v_and_b32_e32 v28, 0xffff0000, v28
	v_lshlrev_b32_e32 v35, 16, v29
	v_and_b32_e32 v29, 0xffff0000, v29
	v_lshlrev_b32_e32 v36, 16, v30
	v_and_b32_e32 v30, 0xffff0000, v30
	v_lshlrev_b32_e32 v37, 16, v31
	v_and_b32_e32 v31, 0xffff0000, v31
	v_fma_f32 v28, v3, v27, -v28
	v_fma_f32 v29, v5, v27, -v29
	v_fma_f32 v30, v7, v27, -v30
	v_fma_f32 v34, v2, v27, -v34
	v_fma_f32 v35, v4, v27, -v35
	v_fma_f32 v36, v6, v27, -v36
	v_fma_f32 v37, v8, v27, -v37
	v_fma_f32 v27, v9, v27, -v31
	v_cvt_pk_bf16_f32 v28, v34, v28
	v_cvt_pk_bf16_f32 v29, v35, v29
	v_cvt_pk_bf16_f32 v30, v36, v30
	v_cvt_pk_bf16_f32 v31, v37, v27
	global_store_dwordx4 v[32:33], v[28:31], off
	s_and_saveexec_b64 s[40:41], vcc
	s_cbranch_execz .LBB0_642
	s_waitcnt vmcnt(8)
	v_mov_b32_e32 v28, v200
	v_mov_b32_e32 v29, v201
	v_mov_b32_e32 v30, v202
	v_mov_b32_e32 v31, v203
	v_lshlrev_b32_e32 v32, 16, v28
	v_and_b32_e32 v33, 0xffff0000, v28
	v_lshlrev_b32_e32 v28, 16, v29
	v_and_b32_e32 v29, 0xffff0000, v29
	v_lshlrev_b32_e32 v34, 16, v30
	v_and_b32_e32 v35, 0xffff0000, v30
	v_lshlrev_b32_e32 v30, 16, v31
	v_and_b32_e32 v31, 0xffff0000, v31
	v_pk_add_f32 v[2:3], v[2:3], v[32:33]
	v_pk_add_f32 v[4:5], v[4:5], v[28:29]
	v_pk_add_f32 v[6:7], v[6:7], v[34:35]
	v_pk_add_f32 v[8:9], v[8:9], v[30:31]
.LBB0_642:
	s_or_b64 exec, exec, s[40:41]
	v_cmp_lt_i32_e32 vcc, -1, v25
	s_and_saveexec_b64 s[40:41], vcc
	s_cbranch_execz .LBB0_644
	s_waitcnt vmcnt(4)
	v_mov_b32_e32 v28, v216
	v_mov_b32_e32 v29, v217
	v_mov_b32_e32 v30, v218
	v_mov_b32_e32 v31, v219
	v_lshlrev_b32_e32 v32, 16, v28
	v_and_b32_e32 v33, 0xffff0000, v28
	v_lshlrev_b32_e32 v28, 16, v29
	v_and_b32_e32 v29, 0xffff0000, v29
	v_lshlrev_b32_e32 v34, 16, v30
	v_and_b32_e32 v35, 0xffff0000, v30
	v_lshlrev_b32_e32 v30, 16, v31
	v_and_b32_e32 v31, 0xffff0000, v31
	v_pk_add_f32 v[2:3], v[2:3], v[32:33] neg_lo:[0,1] neg_hi:[0,1]
	v_pk_add_f32 v[4:5], v[4:5], v[28:29] neg_lo:[0,1] neg_hi:[0,1]
	v_pk_add_f32 v[6:7], v[6:7], v[34:35] neg_lo:[0,1] neg_hi:[0,1]
	v_pk_add_f32 v[8:9], v[8:9], v[30:31] neg_lo:[0,1] neg_hi:[0,1]
.LBB0_644:
	s_or_b64 exec, exec, s[40:41]
	v_add_co_u32_e32 v28, vcc, 0x34402000, v20
	v_add_u32_e32 v27, 1, v25
	s_nop 0
	v_addc_co_u32_e32 v29, vcc, 0, v21, vcc
	s_nop 0
	v_min_i32_e32 v33, v26, v74
	v_max_i32_e32 v34, 0, v27
	v_sub_u32_e32 v33, v33, v34
	v_cvt_f32_i32_e32 v34, v33
	v_add_co_u32_e32 v32, vcc, 0xfd00000, v18
	v_add_u32_e32 v26, 2, v24
	v_rcp_iflag_f32_e32 v34, v34
	v_addc_co_u32_e32 v33, vcc, 0, v19, vcc
	v_cmp_le_i32_e32 vcc, v26, v74
	s_waitcnt vmcnt(11)
	v_mov_b32_e32 v28, v188
	v_mov_b32_e32 v29, v189
	v_mov_b32_e32 v30, v190
	v_mov_b32_e32 v31, v191
	v_lshlrev_b32_e32 v35, 16, v28
	v_and_b32_e32 v28, 0xffff0000, v28
	v_lshlrev_b32_e32 v36, 16, v29
	v_and_b32_e32 v29, 0xffff0000, v29
	v_lshlrev_b32_e32 v37, 16, v30
	v_and_b32_e32 v30, 0xffff0000, v30
	v_lshlrev_b32_e32 v38, 16, v31
	v_and_b32_e32 v31, 0xffff0000, v31
	v_fma_f32 v28, v3, v34, -v28
	v_fma_f32 v29, v5, v34, -v29
	v_fma_f32 v30, v7, v34, -v30
	v_fma_f32 v31, v9, v34, -v31
	v_fma_f32 v35, v2, v34, -v35
	v_fma_f32 v36, v4, v34, -v36
	v_fma_f32 v37, v6, v34, -v37
	v_fma_f32 v38, v8, v34, -v38
	v_cvt_pk_bf16_f32 v28, v35, v28
	v_cvt_pk_bf16_f32 v29, v36, v29
	v_cvt_pk_bf16_f32 v30, v37, v30
	v_cvt_pk_bf16_f32 v31, v38, v31
	global_store_dwordx4 v[32:33], v[28:31], off offset:1024
	s_and_saveexec_b64 s[40:41], vcc
	s_cbranch_execz .LBB0_646
	s_waitcnt vmcnt(8)
	v_mov_b32_e32 v28, v204
	v_mov_b32_e32 v29, v205
	v_mov_b32_e32 v30, v206
	v_mov_b32_e32 v31, v207
	v_lshlrev_b32_e32 v32, 16, v28
	v_and_b32_e32 v33, 0xffff0000, v28
	v_lshlrev_b32_e32 v28, 16, v29
	v_and_b32_e32 v29, 0xffff0000, v29
	v_lshlrev_b32_e32 v34, 16, v30
	v_and_b32_e32 v35, 0xffff0000, v30
	v_lshlrev_b32_e32 v30, 16, v31
	v_and_b32_e32 v31, 0xffff0000, v31
	v_pk_add_f32 v[2:3], v[2:3], v[32:33]
	v_pk_add_f32 v[4:5], v[4:5], v[28:29]
	v_pk_add_f32 v[6:7], v[6:7], v[34:35]
	v_pk_add_f32 v[8:9], v[8:9], v[30:31]
.LBB0_646:
	s_or_b64 exec, exec, s[40:41]
	v_cmp_lt_i32_e32 vcc, -1, v27
	s_and_saveexec_b64 s[40:41], vcc
	s_cbranch_execz .LBB0_648
	s_waitcnt vmcnt(4)
	v_mov_b32_e32 v28, v220
	v_mov_b32_e32 v29, v221
	v_mov_b32_e32 v30, v222
	v_mov_b32_e32 v31, v223
	v_lshlrev_b32_e32 v32, 16, v28
	v_and_b32_e32 v33, 0xffff0000, v28
	v_lshlrev_b32_e32 v28, 16, v29
	v_and_b32_e32 v29, 0xffff0000, v29
	v_lshlrev_b32_e32 v34, 16, v30
	v_and_b32_e32 v35, 0xffff0000, v30
	v_lshlrev_b32_e32 v30, 16, v31
	v_and_b32_e32 v31, 0xffff0000, v31
	v_pk_add_f32 v[2:3], v[2:3], v[32:33] neg_lo:[0,1] neg_hi:[0,1]
	v_pk_add_f32 v[4:5], v[4:5], v[28:29] neg_lo:[0,1] neg_hi:[0,1]
	v_pk_add_f32 v[6:7], v[6:7], v[34:35] neg_lo:[0,1] neg_hi:[0,1]
	v_pk_add_f32 v[8:9], v[8:9], v[30:31] neg_lo:[0,1] neg_hi:[0,1]
.LBB0_648:
	s_or_b64 exec, exec, s[40:41]
	v_add_co_u32_e32 v28, vcc, 0x34404000, v20
	v_add_u32_e32 v27, 2, v25
	s_nop 0
	v_addc_co_u32_e32 v29, vcc, 0, v21, vcc
	s_nop 0
	v_min_i32_e32 v33, v26, v74
	v_max_i32_e32 v34, 0, v27
	v_sub_u32_e32 v33, v33, v34
	v_cvt_f32_i32_e32 v34, v33
	v_add_co_u32_e32 v32, vcc, 0xfd00000, v18
	v_add_u32_e32 v26, 3, v24
	v_rcp_iflag_f32_e32 v34, v34
	v_addc_co_u32_e32 v33, vcc, 0, v19, vcc
	v_cmp_le_i32_e32 vcc, v26, v74
	s_waitcnt vmcnt(11)
	v_mov_b32_e32 v28, v192
	v_mov_b32_e32 v29, v193
	v_mov_b32_e32 v30, v194
	v_mov_b32_e32 v31, v195
	v_lshlrev_b32_e32 v35, 16, v28
	v_and_b32_e32 v28, 0xffff0000, v28
	v_lshlrev_b32_e32 v36, 16, v29
	v_and_b32_e32 v29, 0xffff0000, v29
	v_lshlrev_b32_e32 v37, 16, v30
	v_and_b32_e32 v30, 0xffff0000, v30
	v_lshlrev_b32_e32 v38, 16, v31
	v_and_b32_e32 v31, 0xffff0000, v31
	v_fma_f32 v28, v3, v34, -v28
	v_fma_f32 v29, v5, v34, -v29
	v_fma_f32 v30, v7, v34, -v30
	v_fma_f32 v31, v9, v34, -v31
	v_fma_f32 v35, v2, v34, -v35
	v_fma_f32 v36, v4, v34, -v36
	v_fma_f32 v37, v6, v34, -v37
	v_fma_f32 v38, v8, v34, -v38
	v_cvt_pk_bf16_f32 v28, v35, v28
	v_cvt_pk_bf16_f32 v29, v36, v29
	v_cvt_pk_bf16_f32 v30, v37, v30
	v_cvt_pk_bf16_f32 v31, v38, v31
	global_store_dwordx4 v[32:33], v[28:31], off offset:2048
	s_and_saveexec_b64 s[40:41], vcc
	s_cbranch_execz .LBB0_650
	s_waitcnt vmcnt(8)
	v_mov_b32_e32 v28, v208
	v_mov_b32_e32 v29, v209
	v_mov_b32_e32 v30, v210
	v_mov_b32_e32 v31, v211
	v_lshlrev_b32_e32 v32, 16, v28
	v_and_b32_e32 v33, 0xffff0000, v28
	v_lshlrev_b32_e32 v28, 16, v29
	v_and_b32_e32 v29, 0xffff0000, v29
	v_lshlrev_b32_e32 v34, 16, v30
	v_and_b32_e32 v35, 0xffff0000, v30
	v_lshlrev_b32_e32 v30, 16, v31
	v_and_b32_e32 v31, 0xffff0000, v31
	v_pk_add_f32 v[2:3], v[2:3], v[32:33]
	v_pk_add_f32 v[4:5], v[4:5], v[28:29]
	v_pk_add_f32 v[6:7], v[6:7], v[34:35]
	v_pk_add_f32 v[8:9], v[8:9], v[30:31]
.LBB0_650:
	s_or_b64 exec, exec, s[40:41]
	v_cmp_lt_i32_e32 vcc, -1, v27
	s_and_saveexec_b64 s[40:41], vcc
	s_cbranch_execz .LBB0_652
	s_waitcnt vmcnt(4)
	v_mov_b32_e32 v28, v224
	v_mov_b32_e32 v29, v225
	v_mov_b32_e32 v30, v226
	v_mov_b32_e32 v31, v227
	v_lshlrev_b32_e32 v32, 16, v28
	v_and_b32_e32 v33, 0xffff0000, v28
	v_lshlrev_b32_e32 v28, 16, v29
	v_and_b32_e32 v29, 0xffff0000, v29
	v_lshlrev_b32_e32 v34, 16, v30
	v_and_b32_e32 v35, 0xffff0000, v30
	v_lshlrev_b32_e32 v30, 16, v31
	v_and_b32_e32 v31, 0xffff0000, v31
	v_pk_add_f32 v[2:3], v[2:3], v[32:33] neg_lo:[0,1] neg_hi:[0,1]
	v_pk_add_f32 v[4:5], v[4:5], v[28:29] neg_lo:[0,1] neg_hi:[0,1]
	v_pk_add_f32 v[6:7], v[6:7], v[34:35] neg_lo:[0,1] neg_hi:[0,1]
	v_pk_add_f32 v[8:9], v[8:9], v[30:31] neg_lo:[0,1] neg_hi:[0,1]
.LBB0_652:
	s_or_b64 exec, exec, s[40:41]
	v_add_co_u32_e32 v20, vcc, 0x34406000, v20
	v_add_u32_e32 v32, 4, v24
	s_nop 0
	v_addc_co_u32_e32 v21, vcc, 0, v21, vcc
	s_nop 0
	v_add_u32_e32 v20, 3, v25
	v_min_i32_e32 v21, v26, v74
	v_max_i32_e32 v24, 0, v20
	v_sub_u32_e32 v21, v21, v24
	v_cvt_f32_i32_e32 v21, v21
	v_add_co_u32_e32 v18, vcc, 0xfd00000, v18
	v_rcp_iflag_f32_e32 v21, v21
	s_nop 0
	v_addc_co_u32_e32 v19, vcc, 0, v19, vcc
	v_cmp_le_i32_e32 vcc, v32, v74
	s_waitcnt vmcnt(11)
	v_mov_b32_e32 v28, v196
	v_mov_b32_e32 v29, v197
	v_mov_b32_e32 v30, v198
	v_mov_b32_e32 v31, v199
	v_lshlrev_b32_e32 v24, 16, v28
	v_and_b32_e32 v25, 0xffff0000, v28
	v_lshlrev_b32_e32 v26, 16, v29
	v_and_b32_e32 v27, 0xffff0000, v29
	v_lshlrev_b32_e32 v28, 16, v30
	v_and_b32_e32 v29, 0xffff0000, v30
	v_lshlrev_b32_e32 v30, 16, v31
	v_and_b32_e32 v31, 0xffff0000, v31
	v_fma_f32 v24, v2, v21, -v24
	v_fma_f32 v25, v3, v21, -v25
	v_fma_f32 v26, v4, v21, -v26
	v_fma_f32 v27, v5, v21, -v27
	v_fma_f32 v28, v6, v21, -v28
	v_fma_f32 v29, v7, v21, -v29
	v_fma_f32 v30, v8, v21, -v30
	v_fma_f32 v21, v9, v21, -v31
	v_cvt_pk_bf16_f32 v24, v24, v25
	v_cvt_pk_bf16_f32 v25, v26, v27
	v_cvt_pk_bf16_f32 v26, v28, v29
	v_cvt_pk_bf16_f32 v27, v30, v21
	global_store_dwordx4 v[18:19], v[24:27], off offset:3072
	s_and_saveexec_b64 s[40:41], vcc
	s_cbranch_execz .LBB0_654
	s_waitcnt vmcnt(8)
	v_mov_b32_e32 v24, v212
	v_mov_b32_e32 v25, v213
	v_mov_b32_e32 v26, v214
	v_mov_b32_e32 v27, v215
	v_lshlrev_b32_e32 v18, 16, v24
	v_and_b32_e32 v19, 0xffff0000, v24
	v_lshlrev_b32_e32 v24, 16, v25
	v_and_b32_e32 v25, 0xffff0000, v25
	v_lshlrev_b32_e32 v28, 16, v26
	v_and_b32_e32 v29, 0xffff0000, v26
	v_lshlrev_b32_e32 v26, 16, v27
	v_and_b32_e32 v27, 0xffff0000, v27
	v_pk_add_f32 v[2:3], v[2:3], v[18:19]
	v_pk_add_f32 v[4:5], v[4:5], v[24:25]
	v_pk_add_f32 v[6:7], v[6:7], v[28:29]
	v_pk_add_f32 v[8:9], v[8:9], v[26:27]
.LBB0_654:
	s_or_b64 exec, exec, s[40:41]
	v_cmp_lt_i32_e32 vcc, -1, v20
	s_and_saveexec_b64 s[40:41], vcc
	s_cbranch_execz .LBB0_639
	s_waitcnt vmcnt(4)
	v_mov_b32_e32 v18, v228
	v_mov_b32_e32 v19, v229
	v_mov_b32_e32 v20, v230
	v_mov_b32_e32 v21, v231
	v_lshlrev_b32_e32 v24, 16, v18
	v_and_b32_e32 v25, 0xffff0000, v18
	v_lshlrev_b32_e32 v18, 16, v19
	v_and_b32_e32 v19, 0xffff0000, v19
	v_lshlrev_b32_e32 v26, 16, v20
	v_and_b32_e32 v27, 0xffff0000, v20
	v_lshlrev_b32_e32 v20, 16, v21
	v_and_b32_e32 v21, 0xffff0000, v21
	v_pk_add_f32 v[2:3], v[2:3], v[24:25] neg_lo:[0,1] neg_hi:[0,1]
	v_pk_add_f32 v[4:5], v[4:5], v[18:19] neg_lo:[0,1] neg_hi:[0,1]
	v_pk_add_f32 v[6:7], v[6:7], v[26:27] neg_lo:[0,1] neg_hi:[0,1]
	v_pk_add_f32 v[8:9], v[8:9], v[20:21] neg_lo:[0,1] neg_hi:[0,1]
	s_branch .LBB0_639
